# v21 plus converter section of waves 0-3 at raised priority
# speedup vs baseline: 1.0252x; 1.0252x over previous
.LBB0_538:
	v_cndmask_b32_e64 v2, 0, 1, s[20:21]
	v_cmp_ne_u32_e64 s[6:7], 1, v2
	s_andn2_b64 vcc, exec, s[20:21]
	s_cbranch_vccnz .LBB0_551
	s_setprio 3
	s_cmp_lt_i32 s33, 0
	s_cbranch_scc0 .LBB0_550
	s_cmp_gt_i32 s15, 0x17fff
	s_cbranch_scc1 .LBB0_551

.LBB0_546:
	s_and_b64 vcc, exec, s[6:7]
	s_cbranch_vccnz .LBB0_566
	s_setprio 3
	s_cmp_lt_i32 s33, 0
	s_cbranch_scc0 .LBB0_565
	s_cmp_gt_i32 s59, 0x17fff
	s_cbranch_scc1 .LBB0_566

.LBB0_1433:
	v_cndmask_b32_e64 v2, 0, 1, s[24:25]
	v_cmp_ne_u32_e64 s[8:9], 1, v2
	s_andn2_b64 vcc, exec, s[24:25]
	s_cbranch_vccnz .LBB0_1447
	s_setprio 3
	s_cmp_lt_i32 s70, 0
	s_cbranch_scc0 .LBB0_1446
	s_cmp_gt_i32 s73, 0x17fff
	s_cbranch_scc1 .LBB0_1447

.LBB0_1442:
	s_and_b64 vcc, exec, s[8:9]
	s_cbranch_vccnz .LBB0_1462
	s_setprio 3
	s_cmp_lt_i32 s70, 0
	s_cbranch_scc0 .LBB0_1461
	s_cmp_gt_i32 s72, 0x17fff
	s_cbranch_scc1 .LBB0_1462
